# prologue rows shared by the pool-item and strip waves only (the plain-item waves take none)
# speedup vs baseline: 1.0027x; 1.0027x over previous
; #define GAS __attribute__((address_space(1)))
; __device__ __forceinline__ void p0_prologue(const Frame& F) {
;     ...
;     const bool is_strip = (role == 1) || (role == 2 && ridx < NSTR - 512);
;     if (!is_strip) {
;         const int NRW = NGW - NSTR;
;         const int rw = role == 0 ? ridx : (role == 3 ? 512 + ridx : 1024 + ridx - (NSTR - 512));
;         for (int m = rw; m < M; m += 2 * NRW) {
;             const int m2 = m + NRW; const bool two = m2 < M;
;             const GAS f32x4* xr = (const GAS f32x4*)(x + (size_t)m * D) + F.lane; const GAS f32x4* xr2 = (const GAS f32x4*)(x + (size_t)(two ? m2 : m) * D) + F.lane; f32x4 v[4], v2[4]; float s = 0.f, s2 = 0.f;
.LBB0_145:
	s_cmpk_lt_i32 s16, 0x180
	s_cselect_b64 s[4:5], -1, 0
	s_load_dwordx2 s[26:27], s[76:77], 0
	s_waitcnt lgkmcnt(0)
	s_and_b32 s3, s100, 3
	s_lshr_b32 s16, s100, 2
	s_cmp_eq_u32 s3, 3
	s_cbranch_scc1 .LBB0_161
	s_cmp_lg_u32 s3, 2
	s_cbranch_scc1 .Lrw_ok
	s_cmpk_gt_u32 s16, 0x17f
	s_cbranch_scc1 .LBB0_161
.Lrw_ok:
	s_lshl_b32 s3, s3, 9
	s_add_i32 s16, s16, s3
.LBB0_149:
.LBB0_150:
.LBB0_151:
.LBB0_152:
	s_cmpk_gt_i32 s16, 0x3fff
	s_cbranch_scc1 .LBB0_161
	s_waitcnt vmcnt(15)
	v_mbcnt_lo_u32_b32 v2, -1, 0
	v_mbcnt_hi_u32_b32 v2, -1, v2
	v_and_b32_e32 v3, 64, v2
	v_add_u32_e32 v3, 64, v3
	s_waitcnt vmcnt(13)
	v_xor_b32_e32 v4, 1, v2
	v_cmp_lt_i32_e32 vcc, v4, v3
	v_mov_b32_e32 v1, 0
	s_movk_i32 s2, 0x580
	v_cndmask_b32_e32 v4, v2, v4, vcc
	v_lshlrev_b32_e32 v32, 2, v4
	v_xor_b32_e32 v4, 2, v2
	v_cmp_lt_i32_e32 vcc, v4, v3
	s_mov_b64 s[4:5], 0x5e00000
	v_cndmask_b32_e32 v4, v2, v4, vcc
	v_lshlrev_b32_e32 v33, 2, v4
	v_xor_b32_e32 v4, 4, v2
	v_cmp_lt_i32_e32 vcc, v4, v3
	s_ashr_i32 s17, s16, 31
	s_lshl_b32 s8, s2, 1
	v_cndmask_b32_e32 v4, v2, v4, vcc
	v_lshlrev_b32_e32 v34, 2, v4
	v_xor_b32_e32 v4, 8, v2
	v_cmp_lt_i32_e32 vcc, v4, v3
	s_lshl_b64 s[12:13], s[16:17], 6
	s_mov_b64 s[10:11], 0x7e00000
	v_cndmask_b32_e32 v4, v2, v4, vcc
	v_lshlrev_b32_e32 v35, 2, v4
	v_xor_b32_e32 v4, 16, v2
	v_cmp_lt_i32_e32 vcc, v4, v3
	s_ashr_i32 s9, s8, 31
	s_lshl_b64 s[18:19], s[16:17], 12
	v_cndmask_b32_e32 v4, v2, v4, vcc
	v_lshlrev_b32_e32 v36, 2, v4
	v_xor_b32_e32 v4, 32, v2
	v_cmp_lt_i32_e32 vcc, v4, v3
	v_mov_b32_e32 v3, v1
	v_lshlrev_b32_e32 v0, 4, v68
	v_cndmask_b32_e32 v2, v2, v4, vcc
	v_lshlrev_b32_e32 v37, 2, v2
	v_lshlrev_b32_e32 v2, 3, v68
	v_lshl_add_u64 v[4:5], s[14:15], 0, v[2:3]
	s_waitcnt vmcnt(9)
	v_lshl_add_u64 v[22:23], v[4:5], 0, s[4:5]
	v_lshlrev_b32_e32 v4, 2, v68
	v_mov_b32_e32 v5, v1
	v_lshl_add_u64 v[6:7], s[14:15], 0, v[4:5]
	v_lshl_add_u64 v[4:5], s[12:13], 0, v[4:5]
	s_lshl_b64 s[12:13], s[16:17], 11
	v_lshl_add_u64 v[24:25], v[6:7], 0, s[10:11]
	v_lshl_add_u64 v[26:27], v[4:5], 0, s[10:11]
	s_lshl_b64 s[10:11], s[8:9], 6
	s_waitcnt vmcnt(8)
	v_or_b32_e32 v28, s12, v2
	v_mov_b32_e32 v29, s13
	s_lshl_b64 s[12:13], s[8:9], 11
	s_add_u32 s18, s26, s18
	s_addc_u32 s19, s27, s19
	v_lshl_add_u64 v[20:21], s[26:27], 0, v[0:1]
	v_lshl_add_u64 v[0:1], s[18:19], 0, v[0:1]
	s_mov_b64 s[18:19], 0x800
	v_cmp_gt_u32_e64 s[4:5], 16, v68
	v_cmp_eq_u32_e64 s[6:7], 0, v68
	v_lshl_add_u64 v[30:31], v[0:1], 0, s[18:19]
	s_lshl_b64 s[18:19], s[8:9], 12
	s_movk_i32 s3, 0x7fff
	s_mov_b32 s9, 0xffff0000
	s_mov_b32 s17, 0x5e00000
	s_branch .LBB0_156
